# residual GEMM: the last unit's dummy K-tile re-reads now read this workgroup's x tile, so the epilogue's x loads hit L2
# baseline (speedup 1.0000x reference)
; template <class Epi, class Sched, bool ALIGN_EPI>
; __device__ __forceinline__ void gemm_phase(PG8_LAS unsigned char* lds, const Gemm g, const Sched& S, const Epi& E, const int tid) {
;     ...
;         const bool has_next = S.next(ui + 1, nxt);
;         const char* nA = has_next ? (const char*)g.A + (size_t)nxt.pm * tstepA + PG8_ACOL(nxt) : cA; const char* nB = has_next ? (const char*)g.Bt + (size_t)nxt.pn * tstepB : cB;
;         for (int t = 0; t < nt; t += 2) {
;             const bool last = (t == nt - 2);
;             const char* a1 = cA + (size_t)(t + 1) * kstepA;
;             const char* a2 = last ? nA : cA + (size_t)(t + 2) * kstepA; const char* b2 = last ? nB : cB + (size_t)(t + 2) * kstepB;
;             const char* a3 = a2 + kstepA; const char* b3 = b2 + kstepB;
.LBB0_1395:
	s_cmp_eq_u64 s[6:7], 0
	s_cbranch_scc1 .Lres_next_is_real
	v_readlane_b32 s16, v250, 39
	v_readlane_b32 s17, v250, 40
	s_lshl_b32 s8, s49, 5
	s_lshl_b32 s9, s48, 2
	s_add_i32 s8, s8, s9
	s_lshl_b32 s8, s8, 15
	s_add_u32 s16, s16, 0x26b5c000
	s_addc_u32 s17, s17, 0
	s_add_u32 s16, s16, s8
	s_addc_u32 s17, s17, 0
	s_add_u32 s8, s16, 0x10000
	s_addc_u32 s9, s17, 0
